# selected branch PV: V-fragment LDS reads double-buffered in registers (next output tile's reads in flight before the current tile's MFMAs), on top of the layer-1 w_down deferral
# baseline (speedup 1.0000x reference)
; __device__ __forceinline__ void at_pv(f32x16 (&o)[4], int vb, bf16x8 pa0, bf16x8 pa1, bf16x8 pa2, bf16x8 pa3) {
;     ...
;     PV_D0(0); PV_D0(1); PV_D0(2); PV_D0(3);
;     ...
; }
; __device__ __forceinline__ float at_softmax(f32x16& p0, f32x16& p1, float& m_reg, f32x16& negm, float& l_reg, bf16x8& pa0, bf16x8& pa1, bf16x8& pa2, bf16x8& pa3, bool rowsel, bool use_rowsel) {
;     ...
;     { auto rr = __builtin_amdgcn_permlane32_swap(__float_as_uint(ps), __float_as_uint(ps), false, false); ps = __uint_as_float(rr[0]) + __uint_as_float(rr[1]); }
;     l_reg = l_reg * alpha + ps;
.LBB0_858:
	v_add_f32_e32 v16, v16, v17
	v_fmac_f32_e32 v16, v201, v2
	v_add_u32_e32 v2, s17, v199
	ds_read_b64_tr_b16 v[102:103], v2 offset:0x0
	ds_read_b64_tr_b16 v[104:105], v2 offset:0x800
	ds_read_b64_tr_b16 v[106:107], v2 offset:0x1000
	ds_read_b64_tr_b16 v[108:109], v2 offset:0x1800
	ds_read_b64_tr_b16 v[110:111], v2 offset:0x2000
	ds_read_b64_tr_b16 v[112:113], v2 offset:0x2800
	ds_read_b64_tr_b16 v[114:115], v2 offset:0x3000
	ds_read_b64_tr_b16 v[116:117], v2 offset:0x3800
	ds_read_b64_tr_b16 v[202:203], v2 offset:0x200
	ds_read_b64_tr_b16 v[204:205], v2 offset:0xa00
	ds_read_b64_tr_b16 v[206:207], v2 offset:0x1200
	ds_read_b64_tr_b16 v[208:209], v2 offset:0x1a00
	ds_read_b64_tr_b16 v[210:211], v2 offset:0x2200
	ds_read_b64_tr_b16 v[212:213], v2 offset:0x2a00
	ds_read_b64_tr_b16 v[214:215], v2 offset:0x3200
	ds_read_b64_tr_b16 v[216:217], v2 offset:0x3a00
	s_waitcnt lgkmcnt(8)
	s_nop 0
	v_mfma_f32_32x32x16_bf16 v[66:81], v[102:105], v[4:7], v[66:81]
	ds_read_b64_tr_b16 v[102:103], v2 offset:0x400
	ds_read_b64_tr_b16 v[104:105], v2 offset:0xc00
	v_mfma_f32_32x32x16_bf16 v[66:81], v[106:109], v[12:15], v[66:81]
	ds_read_b64_tr_b16 v[106:107], v2 offset:0x1400
	ds_read_b64_tr_b16 v[108:109], v2 offset:0x1c00
	v_mfma_f32_32x32x16_bf16 v[66:81], v[110:113], v[98:101], v[66:81]
	ds_read_b64_tr_b16 v[110:111], v2 offset:0x2400
	ds_read_b64_tr_b16 v[112:113], v2 offset:0x2c00
	v_mfma_f32_32x32x16_bf16 v[66:81], v[114:117], v[8:11], v[66:81]
	ds_read_b64_tr_b16 v[114:115], v2 offset:0x3400
	ds_read_b64_tr_b16 v[116:117], v2 offset:0x3c00
	s_waitcnt lgkmcnt(8)
	v_mfma_f32_32x32x16_bf16 v[50:65], v[202:205], v[4:7], v[50:65]
	ds_read_b64_tr_b16 v[202:203], v2 offset:0x600
	ds_read_b64_tr_b16 v[204:205], v2 offset:0xe00
	v_mfma_f32_32x32x16_bf16 v[50:65], v[206:209], v[12:15], v[50:65]
	ds_read_b64_tr_b16 v[206:207], v2 offset:0x1600
	ds_read_b64_tr_b16 v[208:209], v2 offset:0x1e00
	v_mfma_f32_32x32x16_bf16 v[50:65], v[210:213], v[98:101], v[50:65]
	ds_read_b64_tr_b16 v[210:211], v2 offset:0x2600
	ds_read_b64_tr_b16 v[212:213], v2 offset:0x2e00
	v_mfma_f32_32x32x16_bf16 v[50:65], v[214:217], v[8:11], v[50:65]
	ds_read_b64_tr_b16 v[214:215], v2 offset:0x3600
	ds_read_b64_tr_b16 v[216:217], v2 offset:0x3e00
	s_waitcnt lgkmcnt(8)
	v_mfma_f32_32x32x16_bf16 v[34:49], v[102:105], v[4:7], v[34:49]
	v_mfma_f32_32x32x16_bf16 v[34:49], v[106:109], v[12:15], v[34:49]
	v_mfma_f32_32x32x16_bf16 v[34:49], v[110:113], v[98:101], v[34:49]
	v_mfma_f32_32x32x16_bf16 v[34:49], v[114:117], v[8:11], v[34:49]
	s_waitcnt lgkmcnt(0)
	v_mfma_f32_32x32x16_bf16 v[18:33], v[202:205], v[4:7], v[18:33]
	v_mov_b32_e32 v201, v16
	v_mfma_f32_32x32x16_bf16 v[18:33], v[206:209], v[12:15], v[18:33]
	v_mfma_f32_32x32x16_bf16 v[18:33], v[210:213], v[98:101], v[18:33]
	v_mfma_f32_32x32x16_bf16 v[18:33], v[214:217], v[8:11], v[18:33]
